# speedup vs baseline: 1.0076x; 1.0076x over previous
.LBB3_20:
	s_or_b64 exec, exec, s[10:11]
	global_load_dwordx4 v[20:23], v[20:21], off
	v_lshlrev_b32_e32 v19, 10, v0
	s_load_dwordx2 s[0:1], s[0:1], 0x48
	v_and_b32_e32 v206, 63, v0
	v_mov_b32_e32 v35, 0
	v_and_b32_e32 v34, 0x70000, v19
	v_lshrrev_b32_e32 v209, 6, v0
	s_waitcnt lgkmcnt(0)
	v_lshl_add_u64 v[24:25], s[8:9], 0, v[34:35]
	v_lshlrev_b32_e32 v34, 4, v206
	v_lshl_add_u64 v[180:181], v[24:25], 0, v[34:35]
	v_lshlrev_b32_e32 v24, 14, v209
	v_mov_b32_e32 v25, v35
	v_lshl_add_u64 v[24:25], s[6:7], 0, v[24:25]
	v_lshlrev_b32_e32 v36, 13, v209
	v_lshlrev_b32_e32 v178, 3, v206
	v_or_b32_e32 v186, 0x200, v0
	v_or_b32_e32 v185, 0x600, v0
	v_or_b32_e32 v184, 0xa00, v0
	v_or_b32_e32 v183, 0xe00, v0
	v_lshl_add_u64 v[126:127], v[24:25], 0, v[34:35]
	v_and_b32_e32 v205, 31, v0
	v_bfe_u32 v208, v0, 5, 1
	global_load_dwordx4 v[38:41], v[126:127], off
	global_load_dwordx4 v[42:45], v[126:127], off offset:1024
	global_load_dwordx4 v[46:49], v[126:127], off offset:2048
	global_load_dwordx4 v[50:53], v[126:127], off offset:3072
	s_movk_i32 s3, 0x2000
	v_add_co_u32_e32 v128, vcc, s3, v126
	s_movk_i32 s3, 0x1000
	s_nop 0
	v_addc_co_u32_e32 v129, vcc, 0, v127, vcc
	global_load_dwordx4 v[54:57], v[128:129], off offset:-4096
	v_add_co_u32_e32 v24, vcc, s3, v126
	s_mov_b32 s14, 0
	s_nop 0
	v_addc_co_u32_e32 v25, vcc, 0, v127, vcc
	global_load_dwordx4 v[58:61], v[24:25], off offset:1024
	global_load_dwordx4 v[62:65], v[24:25], off offset:2048
	global_load_dwordx4 v[98:101], v[24:25], off offset:3072
	v_readfirstlane_b32 s6, v209
	s_nop 3
	s_cmp_lt_u32 s6, 4
	s_cbranch_scc1 .Lmy_ffn_noprio
	s_setprio 1
.Lmy_ffn_noprio:
	s_lshl_b32 s6, s6, 13
	s_cmp_lg_u32 0, -1
	s_cselect_b32 s7, 0, 0
	s_add_i32 s10, s7, s6
	s_mov_b64 s[6:7], 0x2000
	s_add_i32 s8, s10, 0x13400
	v_lshl_add_u64 v[24:25], v[180:181], 0, s[6:7]
	s_mov_b32 s9, m0
	s_mov_b32 m0, s8
	s_nop 0
	global_load_lds_dwordx4 v[24:25], off
	s_mov_b32 m0, s9
	s_mov_b64 s[8:9], 0xa000
	v_lshl_add_u64 v[24:25], v[180:181], 0, s[8:9]
	s_add_i32 s8, s10, 0x13800
	s_mov_b32 s9, m0
	s_mov_b32 m0, s8
	s_nop 0
	global_load_lds_dwordx4 v[24:25], off
	s_mov_b32 m0, s9
	s_mov_b64 s[8:9], 0x2400
	s_add_i32 s11, s10, 0x13c00
	v_lshl_add_u64 v[24:25], v[180:181], 0, s[8:9]
	s_mov_b32 s8, m0
	s_mov_b32 m0, s11
	s_nop 0
	global_load_lds_dwordx4 v[24:25], off
	s_mov_b32 m0, s8
	s_mov_b64 s[8:9], 0xa400
	v_lshl_add_u64 v[24:25], v[180:181], 0, s[8:9]
	s_add_i32 s8, s10, 0x14000
	s_mov_b32 s9, m0
	s_mov_b32 m0, s8
	s_nop 0
	global_load_lds_dwordx4 v[24:25], off
	s_mov_b32 m0, s9
	s_mov_b64 s[8:9], 0x2800
	s_add_i32 s11, s10, 0x14400
	v_lshl_add_u64 v[24:25], v[180:181], 0, s[8:9]
	s_mov_b32 s8, m0
	s_mov_b32 m0, s11
	s_nop 0
	global_load_lds_dwordx4 v[24:25], off
	s_mov_b32 m0, s8
	s_mov_b64 s[8:9], 0xa800
	v_lshl_add_u64 v[24:25], v[180:181], 0, s[8:9]
	s_add_i32 s8, s10, 0x14800
	s_mov_b32 s9, m0
	s_mov_b32 m0, s8
	s_nop 0
	global_load_lds_dwordx4 v[24:25], off
	s_mov_b32 m0, s9
	s_mov_b64 s[8:9], 0x2c00
	s_add_i32 s11, s10, 0x14c00
	v_lshl_add_u64 v[24:25], v[180:181], 0, s[8:9]
	s_mov_b32 s8, m0
	s_mov_b32 m0, s11
	s_nop 0
	global_load_lds_dwordx4 v[24:25], off
	s_mov_b32 m0, s8
	s_mov_b64 s[8:9], 0xac00
	v_lshl_add_u64 v[24:25], v[180:181], 0, s[8:9]
	s_add_i32 s9, 0, 0x11400
	v_lshl_add_u32 v19, v37, 2, s9
	s_add_i32 s10, s10, 0x15000
	s_mov_b32 s8, m0
	s_mov_b32 m0, s10
	s_nop 0
	global_load_lds_dwordx4 v[24:25], off
	s_mov_b32 m0, s8
	s_waitcnt vmcnt(8)
	ds_write_b128 v19, v[20:23]
	v_lshrrev_b32_e32 v19, 5, v0
	v_mul_u32_u24_e32 v19, 0x410, v19
	v_and_b32_e32 v18, 0x1f0, v18
	v_add3_u32 v19, 0, v19, v18
	ds_write_b128 v19, v[14:17] offset:512
	v_lshrrev_b32_e32 v14, 5, v186
	v_mul_u32_u24_e32 v14, 0x410, v14
	v_add3_u32 v14, 0, v14, v18
	ds_write_b128 v14, v[6:9] offset:512
	v_lshrrev_b32_e32 v6, 5, v182
	v_mul_u32_u24_e32 v6, 0x410, v6
	v_add3_u32 v6, 0, v6, v18
	s_movk_i32 s10, 0x410
	ds_write_b128 v6, v[2:5] offset:512
	v_lshrrev_b32_e32 v2, 5, v185
	v_mul_u32_u24_e32 v2, 0x410, v2
	v_mad_u32_u24 v189, v205, s10, 0
	v_add3_u32 v2, 0, v2, v18
	v_lshl_add_u32 v202, v208, 4, v189
	ds_write_b128 v2, v[10:13] offset:512
	s_waitcnt lgkmcnt(0)
	s_barrier
	ds_read_b128 v[2:5], v202 offset:512
	ds_read_b128 v[102:105], v202 offset:544
	ds_read_b128 v[6:9], v202 offset:33792
	ds_read_b128 v[106:109], v202 offset:33824
	v_mul_u32_u24_e32 v187, 0x410, v205
	global_load_dwordx4 v[110:113], v[128:129], off
	s_waitcnt vmcnt(8) lgkmcnt(3)
	v_mfma_f32_32x32x16_f16 v[18:33], v[38:41], v[2:5], 0
	ds_read_b128 v[114:117], v202 offset:576
	ds_read_b128 v[118:121], v202 offset:33856
	s_waitcnt lgkmcnt(3)
	v_mfma_f32_32x32x16_f16 v[2:17], v[38:41], v[6:9], 0
	global_load_dwordx4 v[38:41], v[128:129], off offset:1024
	s_waitcnt vmcnt(8)
	v_mfma_f32_32x32x16_f16 v[18:33], v[42:45], v[102:105], v[18:33]
	ds_read_b128 v[102:105], v202 offset:608
	ds_read_b128 v[122:125], v202 offset:33888
	s_waitcnt lgkmcnt(4)
	v_mfma_f32_32x32x16_f16 v[2:17], v[42:45], v[106:109], v[2:17]
	global_load_dwordx4 v[42:45], v[128:129], off offset:2048
	s_waitcnt vmcnt(8) lgkmcnt(3)
	v_mfma_f32_32x32x16_f16 v[18:33], v[46:49], v[114:117], v[18:33]
	ds_read_b128 v[106:109], v202 offset:640
	ds_read_b128 v[114:117], v202 offset:33920
	s_waitcnt lgkmcnt(4)
	v_mfma_f32_32x32x16_f16 v[2:17], v[46:49], v[118:121], v[2:17]
	global_load_dwordx4 v[46:49], v[128:129], off offset:3072
	s_waitcnt vmcnt(8) lgkmcnt(3)
	v_mfma_f32_32x32x16_f16 v[18:33], v[50:53], v[102:105], v[18:33]
	ds_read_b128 v[102:105], v202 offset:672
	ds_read_b128 v[118:121], v202 offset:33952
	s_waitcnt lgkmcnt(4)
	v_mfma_f32_32x32x16_f16 v[2:17], v[50:53], v[122:125], v[2:17]
	s_movk_i32 s8, 0x3000
	v_add_co_u32_e32 v126, vcc, s8, v126
	s_waitcnt vmcnt(7) lgkmcnt(3)
	v_mfma_f32_32x32x16_f16 v[18:33], v[54:57], v[106:109], v[18:33]
	v_addc_co_u32_e32 v127, vcc, 0, v127, vcc
	global_load_dwordx4 v[50:53], v[126:127], off
	ds_read_b128 v[106:109], v202 offset:704
	ds_read_b128 v[122:125], v202 offset:33984
	s_waitcnt lgkmcnt(4)
	v_mfma_f32_32x32x16_f16 v[2:17], v[54:57], v[114:117], v[2:17]
	global_load_dwordx4 v[54:57], v[126:127], off offset:1024
	s_waitcnt vmcnt(8) lgkmcnt(3)
	v_mfma_f32_32x32x16_f16 v[18:33], v[58:61], v[102:105], v[18:33]
	ds_read_b128 v[102:105], v202 offset:736
	ds_read_b128 v[114:117], v202 offset:34016
	s_waitcnt lgkmcnt(4)
	v_mfma_f32_32x32x16_f16 v[2:17], v[58:61], v[118:121], v[2:17]
	global_load_dwordx4 v[58:61], v[126:127], off offset:2048
	s_waitcnt vmcnt(8) lgkmcnt(3)
	v_mfma_f32_32x32x16_f16 v[18:33], v[62:65], v[106:109], v[18:33]
	ds_read_b128 v[106:109], v202 offset:768
	ds_read_b128 v[118:121], v202 offset:34048
	s_waitcnt lgkmcnt(4)
	v_mfma_f32_32x32x16_f16 v[2:17], v[62:65], v[122:125], v[2:17]
	global_load_dwordx4 v[62:65], v[126:127], off offset:3072
	s_waitcnt vmcnt(8) lgkmcnt(3)
	v_mfma_f32_32x32x16_f16 v[18:33], v[98:101], v[102:105], v[18:33]
	ds_read_b128 v[102:105], v202 offset:800
	ds_read_b128 v[122:125], v202 offset:34080
	s_waitcnt lgkmcnt(4)
	v_mfma_f32_32x32x16_f16 v[2:17], v[98:101], v[114:117], v[2:17]
	s_waitcnt vmcnt(7) lgkmcnt(3)
	v_mfma_f32_32x32x16_f16 v[18:33], v[110:113], v[106:109], v[18:33]
	ds_read_b128 v[98:101], v202 offset:832
	ds_read_b128 v[106:109], v202 offset:34112
	s_waitcnt lgkmcnt(4)
	v_mfma_f32_32x32x16_f16 v[2:17], v[110:113], v[118:121], v[2:17]
	s_waitcnt vmcnt(6) lgkmcnt(3)
	v_mfma_f32_32x32x16_f16 v[18:33], v[38:41], v[102:105], v[18:33]
	ds_read_b128 v[102:105], v202 offset:864
	ds_read_b128 v[110:113], v202 offset:34144
	s_waitcnt lgkmcnt(4)
	v_mfma_f32_32x32x16_f16 v[2:17], v[38:41], v[122:125], v[2:17]
	s_waitcnt vmcnt(5) lgkmcnt(3)
	v_mfma_f32_32x32x16_f16 v[18:33], v[42:45], v[98:101], v[18:33]
	ds_read_b128 v[38:41], v202 offset:896
	ds_read_b128 v[98:101], v202 offset:34176
	s_waitcnt lgkmcnt(4)
	v_mfma_f32_32x32x16_f16 v[2:17], v[42:45], v[106:109], v[2:17]
	s_waitcnt vmcnt(4) lgkmcnt(3)
	v_mfma_f32_32x32x16_f16 v[18:33], v[46:49], v[102:105], v[18:33]
	ds_read_b128 v[42:45], v202 offset:928
	ds_read_b128 v[102:105], v202 offset:34208
	s_waitcnt lgkmcnt(4)
	v_mfma_f32_32x32x16_f16 v[2:17], v[46:49], v[110:113], v[2:17]
	s_waitcnt vmcnt(3) lgkmcnt(3)
	v_mfma_f32_32x32x16_f16 v[18:33], v[50:53], v[38:41], v[18:33]
	ds_read_b128 v[38:41], v202 offset:960
	ds_read_b128 v[46:49], v202 offset:34240
	s_waitcnt lgkmcnt(4)
	v_mfma_f32_32x32x16_f16 v[2:17], v[50:53], v[98:101], v[2:17]
	s_waitcnt vmcnt(2) lgkmcnt(3)
	v_mfma_f32_32x32x16_f16 v[18:33], v[54:57], v[42:45], v[18:33]
	ds_read_b128 v[42:45], v202 offset:992
	ds_read_b128 v[50:53], v202 offset:34272
	s_waitcnt lgkmcnt(4)
	v_mfma_f32_32x32x16_f16 v[2:17], v[54:57], v[102:105], v[2:17]
	s_waitcnt vmcnt(1) lgkmcnt(3)
	v_mfma_f32_32x32x16_f16 v[18:33], v[58:61], v[38:41], v[18:33]
	s_waitcnt lgkmcnt(2)
	v_mfma_f32_32x32x16_f16 v[2:17], v[58:61], v[46:49], v[2:17]
	s_waitcnt vmcnt(0) lgkmcnt(1)
	v_mfma_f32_32x32x16_f16 v[18:33], v[62:65], v[42:45], v[18:33]
	s_waitcnt lgkmcnt(0)
	v_mfma_f32_32x32x16_f16 v[2:17], v[62:65], v[50:53], v[2:17]
	v_and_b32_e32 v188, 0xfc, v37
	v_lshl_add_u32 v35, v188, 1, 0
	v_cvt_pk_f16_f32 v39, v92, v93
	v_cvt_pk_f16_f32 v38, v90, v91
	v_mad_u32_u24 v37, v209, s10, v35
	ds_write_b64 v37, v[38:39]
	v_lshrrev_b32_e32 v37, 6, v186
	v_cvt_pk_f16_f32 v39, v96, v97
	v_cvt_pk_f16_f32 v38, v94, v95
	v_mad_u32_u24 v40, v37, s10, v35
	v_lshrrev_b32_e32 v44, 6, v182
	ds_write_b64 v40, v[38:39]
	v_cvt_pk_f16_f32 v39, v88, v89
	v_cvt_pk_f16_f32 v38, v86, v87
	v_mad_u32_u24 v40, v44, s10, v35
	v_lshrrev_b32_e32 v45, 6, v185
	ds_write_b64 v40, v[38:39]
	v_cvt_pk_f16_f32 v39, v84, v85
	v_cvt_pk_f16_f32 v38, v82, v83
	v_mad_u32_u24 v40, v45, s10, v35
	v_lshrrev_b32_e32 v46, 6, v179
	ds_write_b64 v40, v[38:39]
	v_cvt_pk_f16_f32 v39, v80, v81
	v_cvt_pk_f16_f32 v38, v78, v79
	v_mad_u32_u24 v40, v46, s10, v35
	v_lshrrev_b32_e32 v47, 6, v184
	ds_write_b64 v40, v[38:39]
	v_cvt_pk_f16_f32 v39, v76, v77
	v_cvt_pk_f16_f32 v38, v74, v75
	v_mad_u32_u24 v40, v47, s10, v35
	v_lshrrev_b32_e32 v48, 6, v1
	ds_write_b64 v40, v[38:39]
	v_cvt_pk_f16_f32 v39, v72, v73
	v_cvt_pk_f16_f32 v38, v70, v71
	v_mad_u32_u24 v40, v48, s10, v35
	v_lshrrev_b32_e32 v49, 6, v183
	v_lshlrev_b32_e32 v207, 2, v208
	ds_write_b64 v40, v[38:39]
	v_cvt_pk_f16_f32 v39, v68, v69
	v_cvt_pk_f16_f32 v38, v66, v67
	v_mad_u32_u24 v35, v49, s10, v35
	v_lshl_or_b32 v191, v209, 5, v207
	ds_write_b64 v35, v[38:39]
	v_lshl_add_u32 v35, v191, 2, s9
	s_waitcnt lgkmcnt(0)
	s_barrier
	ds_read_b128 v[38:41], v35
	v_or_b32_e32 v194, 8, v191
	s_mov_b32 s15, 0x9000
	v_or_b32_e32 v200, 16, v191
	v_or_b32_e32 v201, 24, v191
	s_waitcnt lgkmcnt(0)
	v_add_f32_e32 v18, v38, v18
	v_cvt_f16_f32_e32 v35, v18
	v_mov_b32_e32 v18, v19
	v_mov_b32_e32 v19, v20
	v_add_f32_e32 v20, v41, v21
	v_cvt_f16_f32_e32 v20, v20
	v_mov_b32_e32 v42, v39
	v_mov_b32_e32 v43, v40
	v_pk_add_f32 v[18:19], v[42:43], v[18:19]
	v_add_f32_e32 v2, v38, v2
	v_cvt_pk_f16_f32 v19, v18, v19
	v_pack_b32_f16 v18, v35, v19
	v_alignbit_b32 v19, v20, v19, 16
	v_lshl_add_u32 v35, v191, 1, v189
	ds_write_b64 v35, v[18:19] offset:512
	v_cvt_f16_f32_e32 v18, v2
	v_mov_b32_e32 v2, v3
	v_mov_b32_e32 v3, v4
	v_add_f32_e32 v4, v41, v5
	v_cvt_f16_f32_e32 v4, v4
	v_pk_add_f32 v[2:3], v[42:43], v[2:3]
	v_mov_b32_e32 v19, v24
	v_cvt_pk_f16_f32 v3, v2, v3
	v_pack_b32_f16 v2, v18, v3
	v_alignbit_b32 v3, v4, v3, 16
	ds_write_b64 v35, v[2:3] offset:33792
	v_lshl_add_u32 v2, v194, 2, s9
	ds_read_b128 v[2:5], v2
	v_add_co_u32_e32 v24, vcc, s15, v180
	v_mul_u32_u24_e32 v199, 0x410, v209
	v_mul_u32_u24_e32 v198, 0x410, v37
	s_waitcnt lgkmcnt(0)
	v_add_f32_e32 v18, v2, v22
	v_cvt_f16_f32_e32 v20, v18
	v_mov_b32_e32 v38, v3
	v_mov_b32_e32 v39, v4
	v_mov_b32_e32 v18, v23
	v_pk_add_f32 v[18:19], v[38:39], v[18:19]
	v_add_f32_e32 v3, v5, v25
	v_cvt_pk_f16_f32 v4, v18, v19
	v_addc_co_u32_e32 v25, vcc, 0, v181, vcc
	v_pack_b32_f16 v22, v20, v4
	global_load_dwordx4 v[18:21], v[180:181], off
	global_load_dwordx4 v[102:105], v[24:25], off offset:-4096
	v_cvt_f16_f32_e32 v3, v3
	v_add_f32_e32 v2, v2, v6
	v_add_f32_e32 v5, v5, v9
	v_cvt_f16_f32_e32 v5, v5
	v_alignbit_b32 v23, v3, v4, 16
	v_cvt_f16_f32_e32 v4, v2
	v_mov_b32_e32 v2, v7
	v_mov_b32_e32 v3, v8
	v_pk_add_f32 v[2:3], v[38:39], v[2:3]
	ds_write_b64 v35, v[22:23] offset:528
	v_cvt_pk_f16_f32 v3, v2, v3
	v_pack_b32_f16 v2, v4, v3
	v_alignbit_b32 v3, v5, v3, 16
	ds_write_b64 v35, v[2:3] offset:33808
	v_lshl_add_u32 v2, v200, 2, s9
	ds_read_b128 v[2:5], v2
	v_mov_b32_e32 v8, v27
	v_mov_b32_e32 v9, v28
	v_mul_u32_u24_e32 v197, 0x410, v44
	v_mul_u32_u24_e32 v195, 0x410, v45
	s_waitcnt lgkmcnt(0)
	v_add_f32_e32 v6, v2, v26
	v_cvt_f16_f32_e32 v22, v6
	v_mov_b32_e32 v6, v3
	v_add_f32_e32 v3, v5, v29
	v_cvt_f16_f32_e32 v3, v3
	v_mov_b32_e32 v7, v4
	v_pk_add_f32 v[8:9], v[6:7], v[8:9]
	v_add_f32_e32 v2, v2, v10
	v_cvt_pk_f16_f32 v4, v8, v9
	v_add_f32_e32 v5, v5, v13
	v_pack_b32_f16 v8, v22, v4
	v_alignbit_b32 v9, v3, v4, 16
	v_cvt_f16_f32_e32 v4, v2
	v_cvt_f16_f32_e32 v5, v5
	v_mov_b32_e32 v2, v11
	v_mov_b32_e32 v3, v12
	v_pk_add_f32 v[2:3], v[6:7], v[2:3]
	ds_write_b64 v35, v[8:9] offset:544
	v_cvt_pk_f16_f32 v3, v2, v3
	v_pack_b32_f16 v2, v4, v3
	v_alignbit_b32 v3, v5, v3, 16
	ds_write_b64 v35, v[2:3] offset:33824
	v_lshl_add_u32 v2, v201, 2, s9
	ds_read_b128 v[2:5], v2
	v_mov_b32_e32 v8, v31
	v_mov_b32_e32 v9, v32
	s_mov_b32 s9, 0x8000
	v_mul_u32_u24_e32 v196, 0x410, v46
	s_waitcnt lgkmcnt(0)
	v_add_f32_e32 v6, v2, v30
	v_cvt_f16_f32_e32 v10, v6
	v_mov_b32_e32 v6, v3
	v_add_f32_e32 v3, v5, v33
	v_cvt_f16_f32_e32 v3, v3
	v_mov_b32_e32 v7, v4
	v_pk_add_f32 v[8:9], v[6:7], v[8:9]
	v_add_f32_e32 v2, v2, v14
	v_cvt_pk_f16_f32 v4, v8, v9
	v_add_f32_e32 v5, v5, v17
	v_pack_b32_f16 v8, v10, v4
	v_alignbit_b32 v9, v3, v4, 16
	v_cvt_f16_f32_e32 v4, v2
	v_cvt_f16_f32_e32 v5, v5
	v_mov_b32_e32 v2, v15
	v_mov_b32_e32 v3, v16
	v_pk_add_f32 v[2:3], v[6:7], v[2:3]
	v_mul_u32_u24_e32 v193, 0x410, v47
	v_cvt_pk_f16_f32 v3, v2, v3
	v_pack_b32_f16 v2, v4, v3
	v_alignbit_b32 v3, v5, v3, 16
	ds_write_b64 v35, v[2:3] offset:33840
	v_add_co_u32_e32 v2, vcc, s9, v180
	v_mul_u32_u24_e32 v192, 0x410, v48
	v_mul_u32_u24_e32 v190, 0x410, v49
	v_addc_co_u32_e32 v3, vcc, 0, v181, vcc
	ds_write_b64 v35, v[8:9] offset:560
	global_load_dwordx4 v[106:109], v[180:181], off offset:1024
	global_load_dwordx4 v[110:113], v[2:3], off offset:1024
	global_load_dwordx4 v[122:125], v[180:181], off offset:2048
	global_load_dwordx4 v[126:129], v[2:3], off offset:2048
	global_load_dwordx4 v[130:133], v[180:181], off offset:3072
	global_load_dwordx4 v[134:137], v[2:3], off offset:3072
	v_add_co_u32_e32 v2, vcc, s3, v180
	s_nop 1
	v_addc_co_u32_e32 v3, vcc, 0, v181, vcc
	global_load_dwordx4 v[138:141], v[2:3], off
	global_load_dwordx4 v[142:145], v[24:25], off
	global_load_dwordx4 v[150:153], v[2:3], off offset:1024
	global_load_dwordx4 v[154:157], v[24:25], off offset:1024
	global_load_dwordx4 v[158:161], v[2:3], off offset:2048
	global_load_dwordx4 v[162:165], v[24:25], off offset:2048
	global_load_dwordx4 v[166:169], v[2:3], off offset:3072
	global_load_dwordx4 v[210:213], v[24:25], off offset:3072
	s_waitcnt lgkmcnt(0)
	s_barrier
	ds_read_b128 v[2:5], v202
	ds_read_b128 v[114:117], v202 offset:32
	ds_read_b128 v[6:9], v202 offset:33280
	ds_read_b128 v[146:149], v202 offset:33312
	s_add_i32 s9, 0, 0x13400
	v_add3_u32 v204, s9, v36, v34
	s_waitcnt vmcnt(15) lgkmcnt(3)
	v_mfma_f32_32x32x16_f16 v[50:65], v[18:21], v[2:5], 0
	ds_read_b128 v[170:173], v202 offset:64
	ds_read_b128 v[174:177], v202 offset:33344
	ds_read_b128 v[118:121], v204
	ds_read_b128 v[98:101], v204 offset:1024
	s_waitcnt lgkmcnt(5)
	v_mfma_f32_32x32x16_f16 v[34:49], v[18:21], v[6:9], 0
	s_waitcnt vmcnt(14)
	v_mfma_f32_32x32x16_f16 v[18:33], v[102:105], v[2:5], 0
	v_mfma_f32_32x32x16_f16 v[2:17], v[102:105], v[6:9], 0
	s_waitcnt vmcnt(13)
	v_mfma_f32_32x32x16_f16 v[50:65], v[106:109], v[114:117], v[50:65]
	s_waitcnt lgkmcnt(4)
	v_mfma_f32_32x32x16_f16 v[34:49], v[106:109], v[146:149], v[34:49]
	s_waitcnt vmcnt(12)
	v_mfma_f32_32x32x16_f16 v[18:33], v[110:113], v[114:117], v[18:33]
	ds_read_b128 v[214:217], v202 offset:96
	ds_read_b128 v[218:221], v202 offset:33376
	ds_read_b128 v[114:117], v204 offset:2048
	ds_read_b128 v[102:105], v204 offset:3072
	v_mfma_f32_32x32x16_f16 v[2:17], v[110:113], v[146:149], v[2:17]
	s_waitcnt vmcnt(11) lgkmcnt(7)
	v_mfma_f32_32x32x16_f16 v[50:65], v[122:125], v[170:173], v[50:65]
	s_waitcnt lgkmcnt(6)
	v_mfma_f32_32x32x16_f16 v[34:49], v[122:125], v[174:177], v[34:49]
	s_waitcnt vmcnt(10)
	v_mfma_f32_32x32x16_f16 v[18:33], v[126:129], v[170:173], v[18:33]
	ds_read_b128 v[146:149], v202 offset:128
	ds_read_b128 v[170:173], v202 offset:33408
	ds_read_b128 v[122:125], v204 offset:4096
	ds_read_b128 v[106:109], v204 offset:5120
	v_mfma_f32_32x32x16_f16 v[2:17], v[126:129], v[174:177], v[2:17]
	s_waitcnt vmcnt(9) lgkmcnt(7)
	v_mfma_f32_32x32x16_f16 v[50:65], v[130:133], v[214:217], v[50:65]
	s_waitcnt lgkmcnt(6)
	v_mfma_f32_32x32x16_f16 v[34:49], v[130:133], v[218:221], v[34:49]
	ds_read_b128 v[130:133], v202 offset:160
	ds_read_b128 v[174:177], v202 offset:33440
	ds_read_b128 v[126:129], v204 offset:6144
	ds_read_b128 v[110:113], v204 offset:7168
	s_waitcnt vmcnt(8)
	v_mfma_f32_32x32x16_f16 v[18:33], v[134:137], v[214:217], v[18:33]
	v_mfma_f32_32x32x16_f16 v[2:17], v[134:137], v[218:221], v[2:17]
	v_add_co_u32_e32 v226, vcc, s8, v180
	s_mov_b32 s8, 0xb000
	s_nop 0
	v_addc_co_u32_e32 v227, vcc, 0, v181, vcc
	v_add_co_u32_e32 v228, vcc, s8, v180
	s_waitcnt vmcnt(7) lgkmcnt(7)
	v_mfma_f32_32x32x16_f16 v[50:65], v[138:141], v[146:149], v[50:65]
	v_addc_co_u32_e32 v229, vcc, 0, v181, vcc
	s_waitcnt vmcnt(6)
	v_mfma_f32_32x32x16_f16 v[18:33], v[142:145], v[146:149], v[18:33]
	global_load_dwordx4 v[146:149], v[226:227], off
	global_load_dwordx4 v[134:137], v[228:229], off
	s_waitcnt lgkmcnt(6)
	v_mfma_f32_32x32x16_f16 v[34:49], v[138:141], v[170:173], v[34:49]
	ds_read_b128 v[138:141], v202 offset:192
	ds_read_b128 v[214:217], v202 offset:33472
	v_mfma_f32_32x32x16_f16 v[2:17], v[142:145], v[170:173], v[2:17]
	s_waitcnt vmcnt(7) lgkmcnt(5)
	v_mfma_f32_32x32x16_f16 v[50:65], v[150:153], v[130:133], v[50:65]
	s_waitcnt vmcnt(6)
	v_mfma_f32_32x32x16_f16 v[18:33], v[154:157], v[130:133], v[18:33]
	global_load_dwordx4 v[142:145], v[226:227], off offset:1024
	global_load_dwordx4 v[130:133], v[228:229], off offset:1024
	ds_read_b128 v[218:221], v202 offset:224
	ds_read_b128 v[222:225], v202 offset:33504
	s_waitcnt lgkmcnt(6)
	v_mfma_f32_32x32x16_f16 v[34:49], v[150:153], v[174:177], v[34:49]
	v_mfma_f32_32x32x16_f16 v[2:17], v[154:157], v[174:177], v[2:17]
	s_waitcnt vmcnt(7) lgkmcnt(3)
	v_mfma_f32_32x32x16_f16 v[50:65], v[158:161], v[138:141], v[50:65]
	s_waitcnt vmcnt(6)
	v_mfma_f32_32x32x16_f16 v[18:33], v[162:165], v[138:141], v[18:33]
	global_load_dwordx4 v[150:153], v[226:227], off offset:2048
	global_load_dwordx4 v[138:141], v[228:229], off offset:2048
	ds_read_b128 v[174:177], v202 offset:256
	ds_read_b128 v[170:173], v202 offset:33536
	s_waitcnt lgkmcnt(4)
	v_mfma_f32_32x32x16_f16 v[34:49], v[158:161], v[214:217], v[34:49]
	v_mfma_f32_32x32x16_f16 v[2:17], v[162:165], v[214:217], v[2:17]
	global_load_dwordx4 v[158:161], v[226:227], off offset:3072
	global_load_dwordx4 v[154:157], v[228:229], off offset:3072
	s_waitcnt vmcnt(9) lgkmcnt(3)
	v_mfma_f32_32x32x16_f16 v[50:65], v[166:169], v[218:221], v[50:65]
	s_waitcnt lgkmcnt(2)
	v_mfma_f32_32x32x16_f16 v[34:49], v[166:169], v[222:225], v[34:49]
	ds_read_b128 v[166:169], v202 offset:288
	ds_read_b128 v[162:165], v202 offset:33568
	s_waitcnt vmcnt(8)
	v_mfma_f32_32x32x16_f16 v[18:33], v[210:213], v[218:221], v[18:33]
	v_mfma_f32_32x32x16_f16 v[2:17], v[210:213], v[222:225], v[2:17]
	s_mov_b64 s[8:9], 0x4000
	v_add_u32_e32 v203, 0x140, v202
	v_lshl_add_u64 v[180:181], v[180:181], 0, s[8:9]
	s_mov_b64 s[8:9], 0x8000
	s_mov_b64 s[10:11], 0x1000
	s_mov_b64 s[12:13], 0x9000
	v_mov_b32_e32 v210, v203
